# cmp-phase top-n extraction: wave maxima through v_readlane + s_max (no permlane swaps), per-lane pop counters instead of per-round pick-mask updates
# speedup vs baseline: 1.0120x; 1.0120x over previous
; #define LAS __attribute__((address_space(3)))
; #define CE_(i, j) do { const unsigned hi_ = umax_(k[i], k[j]), lo_ = umin_(k[i], k[j]); k[i] = hi_; k[j] = lo_; } while (0)
; __device__ __forceinline__ void sort4_desc(unsigned (&k)[4]) {
;     ...
;     CE_(0, 1); CE_(2, 3); CE_(0, 2); CE_(1, 3); CE_(1, 2);
;     ...
; }
; __device__ __forceinline__ void cmp_phase(Frame& F) {
;     ...
;             unsigned pick[4] = {0u, 0u, 0u, 0u};
; #pragma unroll 1
;             for (int tk = 0; tk < 8; tk += 4) { const LAS float* ir = imp + (8 * F.wave + tk) * 256;
;                 unsigned ka[4], kb2[4], kc[4], kd[4];
; #pragma unroll
;                 for (int q = 0; q < 4; ++q) { const int j = lane + 64 * q; const bool ok = (j >= 1 && j <= cur - 2); const unsigned lo = 7u - (unsigned)q;
;                     ka[q] = ok ? (__builtin_bit_cast(unsigned, ir[j]) & ~3u) + lo : 0u; kb2[q] = ok ? (__builtin_bit_cast(unsigned, ir[256 + j]) & ~3u) + lo : 0u;
;                     kc[q] = ok ? (__builtin_bit_cast(unsigned, ir[512 + j]) & ~3u) + lo : 0u; kd[q] = ok ? (__builtin_bit_cast(unsigned, ir[768 + j]) & ~3u) + lo : 0u; }
;                 sort4_desc(ka); sort4_desc(kb2); sort4_desc(kc); sort4_desc(kd);
;                 unsigned pa = 0u, pb = 0u, pc = 0u, pd = 0u;
.LBB0_1621:
	s_or_b64 exec, exec, s[22:23]
	v_max_u32_e32 v15, v6, v8
	v_min_u32_e32 v8, v6, v8
	v_max_u32_e32 v19, v9, v11
	v_min_u32_e32 v9, v9, v11
	v_max_u32_e32 v6, v15, v19
	v_min_u32_e32 v11, v15, v19
	v_max_u32_e32 v15, v8, v9
	v_min_u32_e32 v8, v8, v9
	v_max_u32_e32 v9, v15, v11
	v_min_u32_e32 v11, v15, v11
	v_max_u32_e32 v15, v7, v12
	v_min_u32_e32 v7, v7, v12
	v_max_u32_e32 v19, v13, v14
	v_min_u32_e32 v13, v13, v14
	v_max_u32_e32 v12, v15, v19
	v_min_u32_e32 v15, v15, v19
	v_max_u32_e32 v19, v7, v13
	v_min_u32_e32 v13, v7, v13
	v_max_u32_e32 v14, v19, v15
	v_min_u32_e32 v15, v19, v15
	v_max_u32_e32 v7, v5, v16
	v_min_u32_e32 v5, v5, v16
	v_max_u32_e32 v19, v17, v18
	v_min_u32_e32 v17, v17, v18
	v_max_u32_e32 v16, v7, v19
	v_min_u32_e32 v7, v7, v19
	v_max_u32_e32 v19, v5, v17
	v_min_u32_e32 v17, v5, v17
	v_max_u32_e32 v18, v19, v7
	v_min_u32_e32 v19, v19, v7
	v_max_u32_e32 v5, v10, v20
	v_min_u32_e32 v7, v10, v20
	v_max_u32_e32 v10, v21, v22
	v_min_u32_e32 v21, v21, v22
	v_max_u32_e32 v20, v5, v10
	v_min_u32_e32 v5, v5, v10
	v_max_u32_e32 v10, v7, v21
	s_xor_b64 s[60:61], s[18:19], -1
	v_min_u32_e32 v21, v7, v21
	v_max_u32_e32 v22, v10, v5
	v_min_u32_e32 v23, v10, v5
	s_mov_b32 s37, 13
	v_mov_b32_e32 v5, 0
	v_mov_b32_e32 v7, 0
	v_mov_b32_e32 v10, 0
	v_and_b32_e32 v25, 3, v6
	v_lshrrev_b32_e64 v239, v25, 8
	v_and_b32_e32 v25, 3, v9
	v_lshrrev_b32_e64 v25, v25, 8
	v_lshl_or_b32 v239, v25, 4, v239
	v_and_b32_e32 v25, 3, v11
	v_lshrrev_b32_e64 v25, v25, 8
	v_lshl_or_b32 v239, v25, 8, v239
	v_and_b32_e32 v25, 3, v8
	v_lshrrev_b32_e64 v25, v25, 8
	v_lshl_or_b32 v239, v25, 12, v239
	v_mov_b32_e32 v243, 0
	v_and_b32_e32 v25, 3, v12
	v_lshrrev_b32_e64 v240, v25, 8
	v_and_b32_e32 v25, 3, v14
	v_lshrrev_b32_e64 v25, v25, 8
	v_lshl_or_b32 v240, v25, 4, v240
	v_and_b32_e32 v25, 3, v15
	v_lshrrev_b32_e64 v25, v25, 8
	v_lshl_or_b32 v240, v25, 8, v240
	v_and_b32_e32 v25, 3, v13
	v_lshrrev_b32_e64 v25, v25, 8
	v_lshl_or_b32 v240, v25, 12, v240
	v_mov_b32_e32 v244, 0
	v_and_b32_e32 v25, 3, v16
	v_lshrrev_b32_e64 v241, v25, 8
	v_and_b32_e32 v25, 3, v18
	v_lshrrev_b32_e64 v25, v25, 8
	v_lshl_or_b32 v241, v25, 4, v241
	v_and_b32_e32 v25, 3, v19
	v_lshrrev_b32_e64 v25, v25, 8
	v_lshl_or_b32 v241, v25, 8, v241
	v_and_b32_e32 v25, 3, v17
	v_lshrrev_b32_e64 v25, v25, 8
	v_lshl_or_b32 v241, v25, 12, v241
	v_mov_b32_e32 v245, 0
	v_and_b32_e32 v25, 3, v20
	v_lshrrev_b32_e64 v242, v25, 8
	v_and_b32_e32 v25, 3, v22
	v_lshrrev_b32_e64 v25, v25, 8
	v_lshl_or_b32 v242, v25, 4, v242
	v_and_b32_e32 v25, 3, v23
	v_lshrrev_b32_e64 v25, v25, 8
	v_lshl_or_b32 v242, v25, 8, v242
	v_and_b32_e32 v25, 3, v21
	v_lshrrev_b32_e64 v25, v25, 8
	v_lshl_or_b32 v242, v25, 12, v242
	v_mov_b32_e32 v246, 0
; __device__ __forceinline__ void topn_round_u(unsigned (&k)[4], unsigned& pm, int lane) {
;     const unsigned wm = wave_max_u(k[0]);
;     const unsigned long long bal = __ballot(k[0] == wm); const int L = __ffsll((long long)bal) - 1;
;     const bool isL = lane == L;
;     pm |= isL ? (8u >> (k[0] & 3u)) : 0u;
;     k[0] = isL ? k[1] : k[0]; k[1] = isL ? k[2] : k[1]; k[2] = isL ? k[3] : k[2]; k[3] = isL ? 0u : k[3];
; }
; __device__ __forceinline__ void cmp_phase(Frame& F) {
;     ...
;                 sort4_desc(ka); sort4_desc(kb2); sort4_desc(kc); sort4_desc(kd);
;                 unsigned pa = 0u, pb = 0u, pc = 0u, pd = 0u;
; #pragma unroll 1
;                 for (int r = 0; r < TOPN - 3; ++r) { topn_round_u(ka, pa, lane); topn_round_u(kb2, pb, lane); topn_round_u(kc, pc, lane); topn_round_u(kd, pd, lane); }
;                 const unsigned bt = 1u << tk;
; #pragma unroll
;                 for (int q = 0; q < 4; ++q) pick[q] |= (((pa >> q) & 1u) ? bt : 0u) | (((pb >> q) & 1u) ? (bt << 1) : 0u) | (((pc >> q) & 1u) ? (bt << 2) : 0u) | (((pd >> q) & 1u) ? (bt << 3) : 0u);
.LBB0_1622:
	v_max_u32_dpp v24, v6, v6 quad_perm:[1,0,3,2] row_mask:0xf bank_mask:0xf bound_ctrl:1
	v_max_u32_dpp v26, v12, v12 quad_perm:[1,0,3,2] row_mask:0xf bank_mask:0xf bound_ctrl:1
	v_max_u32_dpp v28, v16, v16 quad_perm:[1,0,3,2] row_mask:0xf bank_mask:0xf bound_ctrl:1
	v_max_u32_dpp v30, v20, v20 quad_perm:[1,0,3,2] row_mask:0xf bank_mask:0xf bound_ctrl:1
	v_max_u32_dpp v24, v24, v24 quad_perm:[2,3,0,1] row_mask:0xf bank_mask:0xf bound_ctrl:1
	v_max_u32_dpp v26, v26, v26 quad_perm:[2,3,0,1] row_mask:0xf bank_mask:0xf bound_ctrl:1
	v_max_u32_dpp v28, v28, v28 quad_perm:[2,3,0,1] row_mask:0xf bank_mask:0xf bound_ctrl:1
	v_max_u32_dpp v30, v30, v30 quad_perm:[2,3,0,1] row_mask:0xf bank_mask:0xf bound_ctrl:1
	v_max_u32_dpp v24, v24, v24 row_half_mirror row_mask:0xf bank_mask:0xf bound_ctrl:1
	v_max_u32_dpp v26, v26, v26 row_half_mirror row_mask:0xf bank_mask:0xf bound_ctrl:1
	v_max_u32_dpp v28, v28, v28 row_half_mirror row_mask:0xf bank_mask:0xf bound_ctrl:1
	v_max_u32_dpp v30, v30, v30 row_half_mirror row_mask:0xf bank_mask:0xf bound_ctrl:1
	v_max_u32_dpp v24, v24, v24 row_mirror row_mask:0xf bank_mask:0xf bound_ctrl:1
	v_max_u32_dpp v26, v26, v26 row_mirror row_mask:0xf bank_mask:0xf bound_ctrl:1
	v_max_u32_dpp v28, v28, v28 row_mirror row_mask:0xf bank_mask:0xf bound_ctrl:1
	v_max_u32_dpp v30, v30, v30 row_mirror row_mask:0xf bank_mask:0xf bound_ctrl:1
	v_readlane_b32 s18, v24, 0
	v_readlane_b32 s19, v24, 16
	v_readlane_b32 s22, v24, 32
	v_readlane_b32 s23, v24, 48
	v_readlane_b32 s24, v26, 0
	v_readlane_b32 s25, v26, 16
	v_readlane_b32 s48, v26, 32
	v_readlane_b32 s74, v26, 48
	s_max_u32 s18, s18, s19
	s_max_u32 s22, s22, s23
	s_max_u32 s18, s18, s22
	s_max_u32 s24, s24, s25
	s_max_u32 s48, s48, s74
	s_max_u32 s24, s24, s48
	v_readlane_b32 s98, v28, 0
	v_readlane_b32 s99, v28, 16
	v_readlane_b32 s100, v28, 32
	v_readlane_b32 s101, v28, 48
	v_readlane_b32 s75, v30, 0
	v_readlane_b32 s76, v30, 16
	v_readlane_b32 s19, v30, 32
	v_readlane_b32 s22, v30, 48
	v_cmp_eq_u32_e32 vcc, s18, v6
	s_max_u32 s98, s98, s99
	s_max_u32 s100, s100, s101
	s_max_u32 s98, s98, s100
	s_ff1_i32_b64 s23, vcc
	v_cmp_eq_u32_e32 vcc, s23, v143
	s_nop 1
	v_cndmask_b32_e32 v6, v6, v9, vcc
	v_cndmask_b32_e32 v9, v9, v11, vcc
	v_cndmask_b32_e32 v11, v11, v8, vcc
	v_cndmask_b32_e64 v8, v8, 0, vcc
	v_addc_co_u32_e32 v243, vcc, 0, v243, vcc
	v_cmp_eq_u32_e32 vcc, s24, v12
	s_max_u32 s75, s75, s76
	s_max_u32 s19, s19, s22
	s_max_u32 s75, s75, s19
	s_ff1_i32_b64 s23, vcc
	v_cmp_eq_u32_e32 vcc, s23, v143
	s_nop 1
	v_cndmask_b32_e32 v12, v12, v14, vcc
	v_cndmask_b32_e32 v14, v14, v15, vcc
	v_cndmask_b32_e32 v15, v15, v13, vcc
	v_cndmask_b32_e64 v13, v13, 0, vcc
	v_addc_co_u32_e32 v244, vcc, 0, v244, vcc
	v_cmp_eq_u32_e32 vcc, s98, v16
	s_nop 0
	s_ff1_i32_b64 s23, vcc
	v_cmp_eq_u32_e32 vcc, s23, v143
	s_nop 1
	v_cndmask_b32_e32 v16, v16, v18, vcc
	v_cndmask_b32_e32 v18, v18, v19, vcc
	v_cndmask_b32_e32 v19, v19, v17, vcc
	v_cndmask_b32_e64 v17, v17, 0, vcc
	v_addc_co_u32_e32 v245, vcc, 0, v245, vcc
	v_cmp_eq_u32_e32 vcc, s75, v20
	s_nop 0
	s_ff1_i32_b64 s23, vcc
	v_cmp_eq_u32_e32 vcc, s23, v143
	s_nop 1
	v_cndmask_b32_e32 v20, v20, v22, vcc
	v_cndmask_b32_e32 v22, v22, v23, vcc
	v_cndmask_b32_e32 v23, v23, v21, vcc
	v_cndmask_b32_e64 v21, v21, 0, vcc
	v_addc_co_u32_e32 v246, vcc, 0, v246, vcc
	s_add_i32 s37, s37, -1
	s_cmp_eq_u32 s37, 0
	s_cbranch_scc0 .LBB0_1622
	v_lshlrev_b32_e32 v24, 2, v243
	v_bfe_u32 v24, v239, 0, v24
	v_lshrrev_b32_e32 v25, 8, v24
	v_or_b32_e32 v24, v24, v25
	v_lshrrev_b32_e32 v25, 4, v24
	v_or_b32_e32 v24, v24, v25
	v_and_b32_e32 v10, 15, v24
	v_lshlrev_b32_e32 v24, 2, v244
	v_bfe_u32 v24, v240, 0, v24
	v_lshrrev_b32_e32 v25, 8, v24
	v_or_b32_e32 v24, v24, v25
	v_lshrrev_b32_e32 v25, 4, v24
	v_or_b32_e32 v24, v24, v25
	v_and_b32_e32 v7, 15, v24
	v_lshlrev_b32_e32 v24, 2, v245
	v_bfe_u32 v24, v241, 0, v24
	v_lshrrev_b32_e32 v25, 8, v24
	v_or_b32_e32 v24, v24, v25
	v_lshrrev_b32_e32 v25, 4, v24
	v_or_b32_e32 v24, v24, v25
	v_and_b32_e32 v5, 15, v24
	v_lshlrev_b32_e32 v24, 2, v246
	v_bfe_u32 v24, v242, 0, v24
	v_lshrrev_b32_e32 v25, 8, v24
	v_or_b32_e32 v24, v24, v25
	v_lshrrev_b32_e32 v25, 4, v24
	v_or_b32_e32 v24, v24, v25
	v_and_b32_e32 v4, 15, v24
	s_lshl_b32 s18, 1, s36
	s_lshl_b32 s19, 2, s36
	v_bfe_i32 v6, v10, 0, 1
	v_bfe_i32 v8, v7, 0, 1
	v_and_b32_e32 v6, s18, v6
	v_and_b32_e32 v8, s19, v8
	v_or3_b32 v3, v6, v3, v8
	v_bfe_i32 v6, v10, 1, 1
	v_bfe_i32 v8, v7, 1, 1
	s_lshl_b32 s22, 4, s36
	s_lshl_b32 s23, 8, s36
	v_bfe_i32 v9, v5, 0, 1
	v_bfe_i32 v11, v4, 0, 1
	v_and_b32_e32 v6, s18, v6
	v_and_b32_e32 v8, s19, v8
	v_and_b32_e32 v9, s22, v9
	v_and_b32_e32 v11, s23, v11
	v_or3_b32 v2, v6, v2, v8
	v_bfe_i32 v6, v10, 2, 1
	v_bfe_i32 v8, v7, 2, 1
	v_or3_b32 v3, v3, v9, v11
	v_bfe_i32 v9, v5, 1, 1
	v_bfe_i32 v11, v4, 1, 1
	v_and_b32_e32 v6, s18, v6
	v_and_b32_e32 v8, s19, v8
	v_and_b32_e32 v9, s22, v9
	v_and_b32_e32 v11, s23, v11
	v_or3_b32 v1, v6, v1, v8
	v_bfe_i32 v6, v10, 3, 1
	v_bfe_i32 v7, v7, 3, 1
	v_or3_b32 v2, v2, v9, v11
	v_bfe_i32 v9, v5, 2, 1
	v_bfe_i32 v11, v4, 2, 1
	v_and_b32_e32 v6, s18, v6
	v_and_b32_e32 v7, s19, v7
	v_bfe_i32 v5, v5, 3, 1
	v_bfe_i32 v4, v4, 3, 1
	v_and_b32_e32 v9, s22, v9
	v_and_b32_e32 v11, s23, v11
	v_and_b32_e32 v5, s22, v5
	v_and_b32_e32 v4, s23, v4
	v_or3_b32 v0, v6, v0, v7
	v_or3_b32 v1, v1, v9, v11
	v_or3_b32 v0, v0, v5, v4
	s_mov_b64 s[18:19], 0
	s_and_b64 vcc, exec, s[60:61]
	s_cbranch_vccnz .LBB0_1625
	s_mov_b32 s36, 4
	s_branch .LBB0_1605

; __global__ void __launch_bounds__(NTHR, 2) mega_fwd(Args args) {
	.amdhsa_kernel _Z8mega_fwd4Args
		.amdhsa_group_segment_fixed_size 0
		.amdhsa_private_segment_fixed_size 0
		.amdhsa_kernarg_size 520
		.amdhsa_user_sgpr_count 2
		.amdhsa_user_sgpr_dispatch_ptr 0
		.amdhsa_user_sgpr_queue_ptr 0
		.amdhsa_user_sgpr_kernarg_segment_ptr 1
		.amdhsa_user_sgpr_dispatch_id 0
		.amdhsa_user_sgpr_kernarg_preload_length 0
		.amdhsa_user_sgpr_kernarg_preload_offset 0
		.amdhsa_user_sgpr_private_segment_size 0
		.amdhsa_uses_dynamic_stack 0
		.amdhsa_enable_private_segment 0
		.amdhsa_system_sgpr_workgroup_id_x 1
		.amdhsa_system_sgpr_workgroup_id_y 0
		.amdhsa_system_sgpr_workgroup_id_z 0
		.amdhsa_system_sgpr_workgroup_info 0
		.amdhsa_system_vgpr_workitem_id 0
		.amdhsa_next_free_vgpr 256
		.amdhsa_next_free_sgpr 102
		.amdhsa_accum_offset 256
		.amdhsa_reserve_vcc 1
		.amdhsa_float_round_mode_32 0
		.amdhsa_float_round_mode_16_64 0
		.amdhsa_float_denorm_mode_32 3
		.amdhsa_float_denorm_mode_16_64 3
		.amdhsa_dx10_clamp 1
		.amdhsa_ieee_mode 1
		.amdhsa_fp16_overflow 0
		.amdhsa_tg_split 0
		.amdhsa_exception_fp_ieee_invalid_op 0
		.amdhsa_exception_fp_denorm_src 0
		.amdhsa_exception_fp_ieee_div_zero 0
		.amdhsa_exception_fp_ieee_overflow 0
		.amdhsa_exception_fp_ieee_underflow 0
		.amdhsa_exception_fp_ieee_inexact 0
		.amdhsa_exception_int_div_zero 0
	.end_amdhsa_kernel

; __global__ void __launch_bounds__(NTHR, 2) mega_fwd(Args args) {
amdhsa.kernels:
  - .agpr_count:     0
    .args:
      - .offset:         0
        .size:           264
        .value_kind:     by_value
      - .offset:         264
        .size:           4
        .value_kind:     hidden_block_count_x
      - .offset:         268
        .size:           4
        .value_kind:     hidden_block_count_y
      - .offset:         272
        .size:           4
        .value_kind:     hidden_block_count_z
      - .offset:         276
        .size:           2
        .value_kind:     hidden_group_size_x
      - .offset:         278
        .size:           2
        .value_kind:     hidden_group_size_y
      - .offset:         280
        .size:           2
        .value_kind:     hidden_group_size_z
      - .offset:         282
        .size:           2
        .value_kind:     hidden_remainder_x
      - .offset:         284
        .size:           2
        .value_kind:     hidden_remainder_y
      - .offset:         286
        .size:           2
        .value_kind:     hidden_remainder_z
      - .offset:         304
        .size:           8
        .value_kind:     hidden_global_offset_x
      - .offset:         312
        .size:           8
        .value_kind:     hidden_global_offset_y
      - .offset:         320
        .size:           8
        .value_kind:     hidden_global_offset_z
      - .offset:         328
        .size:           2
        .value_kind:     hidden_grid_dims
      - .offset:         384
        .size:           4
        .value_kind:     hidden_dynamic_lds_size
    .group_segment_fixed_size: 0
    .kernarg_segment_align: 8
    .kernarg_segment_size: 520
    .language:       OpenCL C
    .language_version:
      - 2
      - 0
    .max_flat_workgroup_size: 512
    .name:           _Z8mega_fwd4Args
    .private_segment_fixed_size: 0
    .sgpr_count:     108
    .sgpr_spill_count: 25
    .symbol:         _Z8mega_fwd4Args.kd
    .uniform_work_group_size: 1
    .uses_dynamic_stack: false
    .vgpr_count:     256
    .vgpr_spill_count: 0
    .wavefront_size: 64
